# baseline (speedup 1.0000x reference)
.LBB2_31:
	v_add_f32_e32 v188, v188, v192
	v_exp_f32_e32 v49, v40
	v_add_f32_e32 v40, v80, v81
	v_add_f32_e32 v40, v40, v82
	v_add_f32_e32 v40, v40, v83
	v_add_f32_e32 v40, v40, v84
	v_exp_f32_e32 v62, v41
	v_exp_f32_e32 v63, v42
	v_exp_f32_e32 v64, v43
	v_exp_f32_e32 v65, v44
	v_exp_f32_e32 v66, v45
	v_exp_f32_e32 v67, v46
	v_exp_f32_e32 v68, v47
	v_add_f32_e32 v50, v40, v85
	v_cvt_pk_f16_f32 v40, v80, v81
	v_cvt_pk_f16_f32 v41, v82, v83
	v_cvt_pk_f16_f32 v42, v84, v85
	v_cvt_pk_f16_f32 v43, v86, v87
	ds_read_b64_tr_b16 v[44:45], v187 offset:32768
	ds_read_b64_tr_b16 v[46:47], v187 offset:33280
	v_add_f32_e32 v50, v50, v86
	v_add_f32_e32 v54, v50, v87
	ds_read_b64_tr_b16 v[50:51], v187 offset:33792
	ds_read_b64_tr_b16 v[52:53], v187 offset:34304
	s_waitcnt lgkmcnt(2)
	v_mfma_f32_32x32x16_f16 v[0:15], v[40:43], v[44:47], v[0:15]
	ds_read_b64_tr_b16 v[44:45], v187 offset:36864
	ds_read_b64_tr_b16 v[46:47], v187 offset:37376
	v_add_f32_e32 v54, v54, v88
	v_add_f32_e32 v69, v54, v89
	v_cvt_pk_f16_f32 v54, v88, v89
	v_cvt_pk_f16_f32 v55, v90, v91
	v_cvt_pk_f16_f32 v56, v92, v93
	v_cvt_pk_f16_f32 v57, v94, v95
	s_waitcnt lgkmcnt(0)
	v_mfma_f32_32x32x16_f16 v[16:31], v[40:43], v[44:47], v[16:31]
	v_add_f32_e32 v40, v69, v90
	v_add_f32_e32 v40, v40, v91
	v_add_f32_e32 v40, v40, v92
	v_add_f32_e32 v40, v40, v93
	ds_read_b64_tr_b16 v[58:59], v187 offset:37888
	ds_read_b64_tr_b16 v[60:61], v187 offset:38400
	v_add_f32_e32 v40, v40, v94
	v_add_f32_e32 v40, v40, v95
	v_mfma_f32_32x32x16_f16 v[0:15], v[54:57], v[50:53], v[0:15]
	v_add_f32_e32 v40, v40, v32
	v_add_f32_e32 v50, v40, v33
	v_cvt_pk_f16_f32 v40, v32, v33
	v_cvt_pk_f16_f32 v41, v34, v35
	v_cvt_pk_f16_f32 v42, v36, v37
	v_cvt_pk_f16_f32 v43, v38, v39
	ds_read_b64_tr_b16 v[44:45], v187 offset:34816
	ds_read_b64_tr_b16 v[46:47], v187 offset:35328
	s_waitcnt lgkmcnt(2)
	v_mfma_f32_32x32x16_f16 v[16:31], v[54:57], v[58:61], v[16:31]
	v_add_f32_e32 v32, v50, v34
	v_add_f32_e32 v50, v32, v35
	ds_read_b64_tr_b16 v[32:33], v187 offset:35840
	ds_read_b64_tr_b16 v[34:35], v187 offset:36352
	v_add_f32_e32 v36, v50, v36
	v_add_f32_e32 v36, v36, v37
	v_cvt_pk_f16_f32 v50, v49, v62
	v_cvt_pk_f16_f32 v51, v63, v64
	s_waitcnt lgkmcnt(2)
	v_mfma_f32_32x32x16_f16 v[0:15], v[40:43], v[44:47], v[0:15]
	ds_read_b64_tr_b16 v[44:45], v187 offset:38912
	ds_read_b64_tr_b16 v[46:47], v187 offset:39424
	v_cvt_pk_f16_f32 v52, v65, v66
	v_cvt_pk_f16_f32 v53, v67, v68
	ds_read_b64_tr_b16 v[54:55], v187 offset:39936
	ds_read_b64_tr_b16 v[56:57], v187 offset:40448
	v_add_f32_e32 v36, v36, v38
	v_add_f32_e32 v36, v36, v39
	v_add_f32_e32 v36, v36, v49
	s_waitcnt lgkmcnt(2)
	v_mfma_f32_32x32x16_f16 v[16:31], v[40:43], v[44:47], v[16:31]
	v_add_f32_e32 v36, v36, v62
	v_mfma_f32_32x32x16_f16 v[0:15], v[50:53], v[32:35], v[0:15]
	v_add_f32_e32 v32, v36, v63
	v_add_f32_e32 v32, v32, v64
	v_add_f32_e32 v32, v32, v65
	v_add_f32_e32 v32, v32, v66
	v_add_f32_e32 v32, v32, v67
	v_add_f32_e32 v32, v32, v68
	v_add_f32_e32 v32, v188, v32
	s_waitcnt lgkmcnt(0)
	v_mfma_f32_32x32x16_f16 v[16:31], v[50:53], v[54:57], v[16:31]
	v_mov_b32_e32 v33, v32
	s_nop 1
	v_permlane32_swap_b32_e32 v32, v33
	s_and_saveexec_b64 s[2:3], s[0:1]
	v_add_f32_e32 v32, v32, v33
	ds_write_b32 v186, v32 offset:49280
	s_or_b64 exec, exec, s[2:3]
	s_waitcnt lgkmcnt(0)
	ds_read_b128 v[32:35], v48 offset:49280
	ds_read_b128 v[36:39], v48 offset:49312
	s_lshl_b64 s[0:1], s[10:11], 2
	s_add_u32 s0, s6, s0
	s_addc_u32 s1, s7, s1
	s_waitcnt lgkmcnt(1)
	v_rcp_f32_e32 v40, v32
	v_rcp_f32_e32 v41, v33
	s_lshl_b32 s2, s20, 13
	v_rcp_f32_e32 v42, v34
	v_rcp_f32_e32 v43, v35
	s_waitcnt lgkmcnt(0)
	v_rcp_f32_e32 v44, v36
	ds_read_b128 v[32:35], v48 offset:49344
	v_rcp_f32_e32 v45, v37
	v_rcp_f32_e32 v46, v38
	v_rcp_f32_e32 v47, v39
	ds_read_b128 v[36:39], v48 offset:49376
	s_add_i32 s2, s2, 0
	v_lshlrev_b32_e32 v48, 2, v181
	v_add3_u32 v48, s2, v182, v48
	v_mul_f32_e32 v0, v0, v40
	v_mul_f32_e32 v16, v16, v40
	v_add_u32_e32 v40, 0xc800, v48
	ds_write2_b32 v40, v0, v16 offset1:32
	v_mul_f32_e32 v0, v1, v41
	v_mul_f32_e32 v1, v17, v41
	ds_write2_b32 v40, v0, v1 offset0:64 offset1:96
	v_mul_f32_e32 v0, v2, v42
	v_mul_f32_e32 v1, v18, v42
	ds_write2_b32 v40, v0, v1 offset0:128 offset1:160
	v_mul_f32_e32 v0, v3, v43
	v_mul_f32_e32 v1, v19, v43
	s_waitcnt lgkmcnt(4)
	v_rcp_f32_e32 v32, v32
	ds_write2_b32 v40, v0, v1 offset0:192 offset1:224
	v_mul_f32_e32 v0, v4, v44
	v_mul_f32_e32 v1, v20, v44
	v_add_u32_e32 v2, 0xd000, v48
	v_rcp_f32_e32 v33, v33
	ds_write2_b32 v2, v0, v1 offset1:32
	v_mul_f32_e32 v0, v5, v45
	v_mul_f32_e32 v1, v21, v45
	v_rcp_f32_e32 v34, v34
	ds_write2_b32 v2, v0, v1 offset0:64 offset1:96
	v_mul_f32_e32 v0, v6, v46
	v_mul_f32_e32 v1, v22, v46
	v_rcp_f32_e32 v35, v35
	ds_write2_b32 v2, v0, v1 offset0:128 offset1:160
	v_mul_f32_e32 v0, v7, v47
	v_mul_f32_e32 v1, v23, v47
	s_waitcnt lgkmcnt(7)
	v_rcp_f32_e32 v36, v36
	ds_write2_b32 v2, v0, v1 offset0:192 offset1:224
	v_mul_f32_e32 v0, v8, v32
	v_mul_f32_e32 v1, v24, v32
	v_add_u32_e32 v2, 0xd800, v48
	v_rcp_f32_e32 v37, v37
	ds_write2_b32 v2, v0, v1 offset1:32
	v_mul_f32_e32 v0, v9, v33
	v_mul_f32_e32 v1, v25, v33
	v_rcp_f32_e32 v38, v38
	ds_write2_b32 v2, v0, v1 offset0:64 offset1:96
	v_mul_f32_e32 v0, v10, v34
	v_mul_f32_e32 v1, v26, v34
	v_rcp_f32_e32 v39, v39
	ds_write2_b32 v2, v0, v1 offset0:128 offset1:160
	v_mul_f32_e32 v0, v11, v35
	v_mul_f32_e32 v1, v27, v35
	ds_write2_b32 v2, v0, v1 offset0:192 offset1:224
	v_mul_f32_e32 v0, v12, v36
	v_mul_f32_e32 v1, v28, v36
	v_add_u32_e32 v2, 0xe000, v48
	ds_write2_b32 v2, v0, v1 offset1:32
	v_mul_f32_e32 v0, v13, v37
	v_mul_f32_e32 v1, v29, v37
	ds_write2_b32 v2, v0, v1 offset0:64 offset1:96
	v_mul_f32_e32 v0, v14, v38
	v_mul_f32_e32 v1, v30, v38
	ds_write2_b32 v2, v0, v1 offset0:128 offset1:160
	v_mul_f32_e32 v0, v15, v39
	v_mul_f32_e32 v1, v31, v39
	v_and_b32_e32 v8, 0xf0, v185
	ds_write2_b32 v2, v0, v1 offset0:192 offset1:224
	v_add_u32_e32 v14, s2, v8
	s_waitcnt lgkmcnt(0)
	v_lshl_add_u32 v0, v183, 8, v14
	s_lshl_b32 s3, s21, 2
	ds_read_b128 v[16:19], v0 offset:51200
	ds_read_b128 v[20:23], v0 offset:52224
	ds_read_b128 v[24:27], v0 offset:53248
	ds_read_b128 v[28:31], v0 offset:54272
	ds_read_b128 v[32:35], v0 offset:55296
	ds_read_b128 v[36:39], v0 offset:56320
	ds_read_b128 v[40:43], v0 offset:57344
	ds_read_b128 v[44:47], v0 offset:58368
	s_add_u32 s0, s0, s3
	s_addc_u32 s1, s1, 0
	v_lshl_add_u32 v9, v183, 11, v8
	s_waitcnt lgkmcnt(7)
	global_store_dwordx4 v9, v[16:19], s[0:1] sc1
	s_add_u32 s0, s0, 0x2000
	s_addc_u32 s1, s1, 0
	s_waitcnt lgkmcnt(6)
	global_store_dwordx4 v9, v[20:23], s[0:1] sc1
	s_add_u32 s0, s0, 0x2000
	s_addc_u32 s1, s1, 0
	s_waitcnt lgkmcnt(5)
	global_store_dwordx4 v9, v[24:27], s[0:1] sc1
	s_add_u32 s0, s0, 0x2000
	s_addc_u32 s1, s1, 0
	s_waitcnt lgkmcnt(4)
	global_store_dwordx4 v9, v[28:31], s[0:1] sc1
	s_add_u32 s0, s0, 0x2000
	s_addc_u32 s1, s1, 0
	s_waitcnt lgkmcnt(3)
	global_store_dwordx4 v9, v[32:35], s[0:1] sc1
	s_add_u32 s0, s0, 0x2000
	s_addc_u32 s1, s1, 0
	s_waitcnt lgkmcnt(2)
	global_store_dwordx4 v9, v[36:39], s[0:1] sc1
	s_add_u32 s0, s0, 0x2000
	s_addc_u32 s1, s1, 0
	s_waitcnt lgkmcnt(1)
	global_store_dwordx4 v9, v[40:43], s[0:1] sc1
	s_add_u32 s0, s0, 0x2000
	s_addc_u32 s1, s1, 0
	s_waitcnt lgkmcnt(0)
	global_store_dwordx4 v9, v[44:47], s[0:1] sc1
	s_endpgm
